# v73 + GQA loops: V-tile LDS write base hoisted (one vector add per tile instead of two)
# speedup vs baseline: 1.0043x; 1.0008x over previous
; DI f32x16 mfma8(v8i a, v8i b, f32x16 c) { return __builtin_amdgcn_mfma_scale_f32_32x32x64_f8f6f4(a, b, c, 0, 0, 0, 0, 0, 0); }
; DI void attn_unit_a8(unsigned char* lds, const AttnArgs& a) {
;     ...
;     auto gload = [&](int t, u32x2& kreg, u32x2& vreg) __attribute__((always_inline)) {
;         const unsigned char* kp = (t < 64) ? a.klat8 + (size_t)(t * 64 + lrow) * 128 : a.kctx8 + (size_t)((t - 64) * 64 + lrow) * 128;
;         kreg = *(const u32x2*)(kp + 8 * lch);
;         vreg = *(const u32x2*)(vsrc + (size_t)t * 64);
;     };
;     auto lstore = [&](int slot, const u32x2& kreg, const u32x2& vreg) __attribute__((always_inline)) { unsigned char* b = lds + slot * AT_BUFB;
;         *(u32x2*)(b + ldk) = kreg; *(unsigned*)(b + ldv) = vreg.x; *(unsigned*)(b + ldv + 32) = vreg.y; };
;     ...
;     auto step = [&](int t, u32x2& kl, u32x2& vl, const u32x2& ks, const u32x2& vs, f32x16& c0, f32x16& c1, f32x16& n0, f32x16& n1, const int hk, const int wj) __attribute__((always_inline)) {
;         const int slot1 = slot == 2 ? 0 : slot + 1, slot2 = slot1 == 2 ? 0 : slot1 + 1;
;         if (hk == 1) { w_cvt(); w_issue(wj + 1 < AT_NWT ? wj + 1 : AT_NWT - 1); }
;         if (hk == 2) w_store(wj);
;         { const int tn = t + 3; gload(tn < a.t1 ? tn : a.t1 - 1, kl, vl); }
;         const unsigned char* Kb = lds + slot * AT_BUFB; const unsigned char* Kn = lds + slot1 * AT_BUFB;
;         const v8i k0 = kread(Kn, 0), k1 = kread(Kn, 1), v0 = vread(Kb, 0), v1 = vread(Kb, 1);
;         n0 = mfma8(k0, qf8, cinit); n1 = mfma8(k1, qf8, cinit);
;         expsum(c0); expsum(c1);
;         const v8i P = pack8(c0, c1);
;         o0[0] = mfma8(v0, P, o0[0]); o0[1] = mfma8(v1, P, o0[1]);
;         lstore(slot2, ks, vs);
;         __syncthreads();
;         slot = slot1;
;     };
.LBB0_712:
	s_cmpk_gt_i32 s56, 0x43
	s_cbranch_scc1 .LBB0_688
	s_mov_b32 s8, 0
	v_mov_b64_e32 v[80:81], v[48:49]
	v_mov_b64_e32 v[78:79], v[46:47]
	v_mov_b64_e32 v[76:77], v[44:45]
	v_mov_b64_e32 v[74:75], v[42:43]
	v_mov_b64_e32 v[72:73], v[40:41]
	v_mov_b64_e32 v[70:71], v[38:39]
	v_mov_b64_e32 v[68:69], v[36:37]
	v_mov_b64_e32 v[66:67], v[34:35]
	v_mov_b64_e32 v[96:97], v[64:65]
	v_mov_b64_e32 v[94:95], v[62:63]
	v_mov_b64_e32 v[92:93], v[60:61]
	v_mov_b64_e32 v[90:91], v[58:59]
	v_mov_b64_e32 v[88:89], v[56:57]
	v_mov_b64_e32 v[86:87], v[54:55]
	v_mov_b64_e32 v[84:85], v[52:53]
	v_mov_b64_e32 v[82:83], v[50:51]
	v_mov_b32_e32 v236, v154
	v_ashrrev_i32_e32 v237, 31, v154
	v_lshlrev_b64 v[236:237], 7, v[236:237]
	v_lshl_add_u64 v[236:237], v[236:237], 0, v[130:131]
	v_add_u32_e32 v238, 0x1400, v156
.LBB0_714:
	s_min_i32 s4, s56, 64
	s_add_i32 s6, s4, 3
	s_cmp_lt_u32 s56, 61
	s_cselect_b64 s[10:11], -1, 0
	s_lshl_b32 s4, s6, 6
	s_add_i32 s7, s4, 0xfffff000
	s_and_b64 s[12:13], s[10:11], exec
	s_cselect_b32 s4, s4, s7
	s_lshl_b32 s72, s4, 7
	s_add_i32 s4, s8, 1
	s_cmp_lg_u32 s8, 2
	s_mov_b32 s9, s8
	s_cselect_b32 s8, s4, 0
	s_mul_i32 s4, s8, 0x4680
	v_add_u32_e32 v106, s4, v157
	ds_read_b128 v[34:37], v106
	ds_read_b128 v[38:41], v106 offset:16
	s_and_b64 s[10:11], s[10:11], exec
	s_cselect_b32 s10, s58, s60
	s_cselect_b32 s11, s59, s61
	s_ashr_i32 s7, s6, 31
	s_waitcnt lgkmcnt(0)
	v_mfma_f32_32x32x64_f8f6f4 v[50:65], v[34:41], v[98:105], 0
	s_lshl_b64 s[12:13], s[6:7], 6
	s_add_u32 s72, s10, s72
	s_addc_u32 s73, s11, 0
	v_lshl_add_u64 v[34:35], v[236:237], 0, s[72:73]
	v_lshl_add_u64 v[42:43], v[132:133], 0, s[12:13]
	global_load_dwordx2 v[112:113], v[34:35], off
	ds_read_b128 v[34:37], v106 offset:2560
	ds_read_b128 v[38:41], v106 offset:2576
	global_load_dwordx2 v[114:115], v[42:43], off
	s_mulk_i32 s9, 0x4680
	v_add_u32_e32 v42, s9, v157
	v_exp_f32_e32 v82, v82
	v_exp_f32_e32 v83, v83
	v_exp_f32_e32 v86, v86
	v_exp_f32_e32 v87, v87
	v_exp_f32_e32 v90, v90
	v_exp_f32_e32 v91, v91
	v_exp_f32_e32 v94, v94
	v_exp_f32_e32 v95, v95
	v_exp_f32_e32 v124, v66
	v_exp_f32_e32 v125, v67
	v_exp_f32_e32 v146, v70
	v_exp_f32_e32 v147, v71
	v_exp_f32_e32 v74, v74
	v_exp_f32_e32 v75, v75
	v_exp_f32_e32 v78, v78
	v_exp_f32_e32 v79, v79
	ds_read_b128 v[116:119], v42 offset:5120
	ds_read_b128 v[120:123], v42 offset:5136
	ds_read_b128 v[138:141], v42 offset:7680
	ds_read_b128 v[142:145], v42 offset:7696
	v_exp_f32_e32 v84, v84
	v_exp_f32_e32 v85, v85
	v_exp_f32_e32 v88, v88
	v_exp_f32_e32 v89, v89
	v_exp_f32_e32 v92, v92
	v_exp_f32_e32 v93, v93
	v_exp_f32_e32 v96, v96
	v_exp_f32_e32 v97, v97
	v_exp_f32_e32 v126, v68
	v_exp_f32_e32 v127, v69
	v_exp_f32_e32 v148, v72
	v_exp_f32_e32 v149, v73
	v_exp_f32_e32 v76, v76
	v_exp_f32_e32 v77, v77
	v_exp_f32_e32 v80, v80
	v_exp_f32_e32 v81, v81
	v_cvt_scalef32_pk_fp8_f32 v66, v82, v83, s48
	v_cvt_scalef32_pk_fp8_f32 v70, v124, v125, s48
	v_cvt_scalef32_pk_fp8_f32 v67, v86, v87, s48
	v_cvt_scalef32_pk_fp8_f32 v71, v146, v147, s48
	v_cvt_scalef32_pk_fp8_f32 v68, v90, v91, s48
	v_cvt_scalef32_pk_fp8_f32 v72, v74, v75, s48
	v_cvt_scalef32_pk_fp8_f32 v69, v94, v95, s48
	v_cvt_scalef32_pk_fp8_f32 v73, v78, v79, s48
	v_cvt_scalef32_pk_fp8_f32 v66, v84, v85, s48 op_sel:[0,0,0,1]
	v_cvt_scalef32_pk_fp8_f32 v70, v126, v127, s48 op_sel:[0,0,0,1]
	v_cvt_scalef32_pk_fp8_f32 v67, v88, v89, s48 op_sel:[0,0,0,1]
	v_cvt_scalef32_pk_fp8_f32 v71, v148, v149, s48 op_sel:[0,0,0,1]
	v_cvt_scalef32_pk_fp8_f32 v68, v92, v93, s48 op_sel:[0,0,0,1]
	v_cvt_scalef32_pk_fp8_f32 v72, v76, v77, s48 op_sel:[0,0,0,1]
	v_cvt_scalef32_pk_fp8_f32 v69, v96, v97, s48 op_sel:[0,0,0,1]
	v_cvt_scalef32_pk_fp8_f32 v73, v80, v81, s48 op_sel:[0,0,0,1]
	s_waitcnt lgkmcnt(4)
	v_mfma_f32_32x32x64_f8f6f4 v[34:49], v[34:41], v[98:105], 0
	s_addk_i32 s4, 0x4680
	s_cmp_eq_u32 s8, 2
	v_add_f32_e64 v110, v110, v84
	v_add_f32_e64 v111, v111, v85
	v_add_f32_e64 v82, v108, v82
	v_add_f32_e64 v83, v109, v83
	s_cselect_b64 s[6:7], -1, 0
	v_add_f32_e64 v84, v88, v110
	v_add_f32_e64 v85, v89, v111
	v_add_f32_e64 v82, v86, v82
	v_add_f32_e64 v83, v87, v83
	v_add_f32_e64 v84, v92, v84
	v_add_f32_e64 v85, v93, v85
	v_pk_add_f32 v[82:83], v[90:91], v[82:83]
	s_and_b64 s[10:11], s[6:7], exec
	v_pk_add_f32 v[84:85], v[96:97], v[84:85]
	v_pk_add_f32 v[82:83], v[94:95], v[82:83]
	s_cselect_b32 s4, 0, s4
	v_pk_add_f32 v[82:83], v[124:125], v[82:83]
	v_pk_add_f32 v[84:85], v[126:127], v[84:85]
	s_waitcnt lgkmcnt(2)
	v_mfma_f32_32x32x64_f8f6f4 v[18:33], v[116:123], v[66:73], v[18:33]
	s_add_i32 s4, s4, 0
	v_add_f32_e64 v84, v148, v84
	v_add_f32_e64 v85, v149, v85
	v_add_f32_e64 v82, v146, v82
	v_add_f32_e64 v83, v147, v83
	v_add_f32_e64 v76, v76, v84
	v_add_f32_e64 v77, v77, v85
	v_add_f32_e64 v74, v74, v82
	v_add_f32_e64 v75, v75, v83
	v_add_f32_e64 v110, v80, v76
	v_add_f32_e64 v111, v81, v77
	v_add_f32_e64 v108, v78, v74
	v_add_f32_e64 v109, v79, v75
	s_cmpk_gt_u32 s56, 0x42
	s_waitcnt lgkmcnt(0)
	v_mfma_f32_32x32x64_f8f6f4 v[2:17], v[138:145], v[66:73], v[2:17]
	v_add_u32_e32 v66, s4, v155
	s_waitcnt vmcnt(3)
	ds_write_b64 v66, v[134:135]
	v_add_u32_e32 v66, s4, v238
	s_waitcnt vmcnt(2)
	ds_write2_b32 v66, v136, v137 offset1:8
	s_waitcnt lgkmcnt(0)
	s_barrier
; DI f32x16 mfma8(v8i a, v8i b, f32x16 c) { return __builtin_amdgcn_mfma_scale_f32_32x32x64_f8f6f4(a, b, c, 0, 0, 0, 0, 0, 0); }
; DI void attn_unit_a8(unsigned char* lds, const AttnArgs& a) {
;     ...
;     auto gload = [&](int t, u32x2& kreg, u32x2& vreg) __attribute__((always_inline)) {
;         const unsigned char* kp = (t < 64) ? a.klat8 + (size_t)(t * 64 + lrow) * 128 : a.kctx8 + (size_t)((t - 64) * 64 + lrow) * 128;
;         kreg = *(const u32x2*)(kp + 8 * lch);
;         vreg = *(const u32x2*)(vsrc + (size_t)t * 64);
;     };
;     auto lstore = [&](int slot, const u32x2& kreg, const u32x2& vreg) __attribute__((always_inline)) { unsigned char* b = lds + slot * AT_BUFB;
;         *(u32x2*)(b + ldk) = kreg; *(unsigned*)(b + ldv) = vreg.x; *(unsigned*)(b + ldv + 32) = vreg.y; };
;     ...
;     auto step = [&](int t, u32x2& kl, u32x2& vl, const u32x2& ks, const u32x2& vs, f32x16& c0, f32x16& c1, f32x16& n0, f32x16& n1, const int hk, const int wj) __attribute__((always_inline)) {
;         const int slot1 = slot == 2 ? 0 : slot + 1, slot2 = slot1 == 2 ? 0 : slot1 + 1;
;         if (hk == 1) { w_cvt(); w_issue(wj + 1 < AT_NWT ? wj + 1 : AT_NWT - 1); }
;         if (hk == 2) w_store(wj);
;         { const int tn = t + 3; gload(tn < a.t1 ? tn : a.t1 - 1, kl, vl); }
;         const unsigned char* Kb = lds + slot * AT_BUFB; const unsigned char* Kn = lds + slot1 * AT_BUFB;
;         const v8i k0 = kread(Kn, 0), k1 = kread(Kn, 1), v0 = vread(Kb, 0), v1 = vread(Kb, 1);
;         n0 = mfma8(k0, qf8, cinit); n1 = mfma8(k1, qf8, cinit);
;         expsum(c0); expsum(c1);
;         const v8i P = pack8(c0, c1);
;         o0[0] = mfma8(v0, P, o0[0]); o0[1] = mfma8(v1, P, o0[1]);
;         lstore(slot2, ks, vs);
;         __syncthreads();
;         slot = slot1;
;     };
	s_cbranch_scc1 .LBB0_716
	s_min_u32 s4, s56, 63
	s_cmp_lt_u32 s56, 60
	s_cselect_b64 s[10:11], -1, 0
	s_lshl_b32 s4, s4, 6
	s_add_i32 s9, s4, 0x100
	s_add_i32 s14, s4, 0xfffff100
	s_and_b64 s[12:13], s[10:11], exec
	s_cselect_b32 s9, s9, s14
	s_lshl_b32 s74, s9, 7
	s_add_i32 s8, s8, 1
	s_and_b64 s[6:7], s[6:7], exec
	s_cselect_b32 s8, 0, s8
	s_and_b64 s[10:11], s[10:11], exec
	s_cselect_b32 s11, s59, s61
	s_cselect_b32 s10, s58, s60
	s_mul_i32 s6, s8, 0x4680
	s_add_u32 s74, s10, s74
	s_addc_u32 s75, s11, 0
	v_add_u32_e32 v86, s6, v157
	v_lshl_add_u64 v[90:91], v[236:237], 0, s[74:75]
	ds_read_b128 v[66:69], v86 offset:2560
	ds_read_b128 v[70:73], v86 offset:2576
	ds_read_b128 v[82:85], v86
	ds_read_b128 v[86:89], v86 offset:16
	global_load_dwordx2 v[134:135], v[90:91], off
	v_lshl_add_u64 v[90:91], v[132:133], 0, s[4:5]
	global_load_dwordx2 v[136:137], v[90:91], off offset:256
	v_exp_f32_e32 v50, v50
	v_exp_f32_e32 v51, v51
	v_exp_f32_e32 v54, v54
	v_exp_f32_e32 v55, v55
	v_exp_f32_e32 v58, v58
	v_exp_f32_e32 v59, v59
	v_exp_f32_e32 v62, v62
	v_exp_f32_e32 v63, v63
	v_exp_f32_e32 v124, v34
	v_exp_f32_e32 v125, v35
	v_exp_f32_e32 v146, v38
	v_exp_f32_e32 v147, v39
	v_exp_f32_e32 v42, v42
	v_exp_f32_e32 v43, v43
	v_exp_f32_e32 v46, v46
	v_exp_f32_e32 v47, v47
	ds_read_b128 v[116:119], v106 offset:5120
	ds_read_b128 v[120:123], v106 offset:5136
	ds_read_b128 v[138:141], v106 offset:7680
	ds_read_b128 v[142:145], v106 offset:7696
	v_exp_f32_e32 v52, v52
	v_exp_f32_e32 v53, v53
	v_exp_f32_e32 v56, v56
	v_exp_f32_e32 v57, v57
	v_exp_f32_e32 v60, v60
	v_exp_f32_e32 v61, v61
	v_exp_f32_e32 v64, v64
	v_exp_f32_e32 v65, v65
	v_exp_f32_e32 v126, v36
	v_exp_f32_e32 v127, v37
	v_exp_f32_e32 v148, v40
	v_exp_f32_e32 v149, v41
	v_exp_f32_e32 v44, v44
	v_exp_f32_e32 v45, v45
	v_exp_f32_e32 v48, v48
	v_exp_f32_e32 v49, v49
	s_waitcnt lgkmcnt(6)
	v_mfma_f32_32x32x64_f8f6f4 v[66:81], v[66:73], v[98:105], 0
	v_cvt_scalef32_pk_fp8_f32 v34, v50, v51, s48
	v_cvt_scalef32_pk_fp8_f32 v38, v124, v125, s48
	v_cvt_scalef32_pk_fp8_f32 v35, v54, v55, s48
	v_cvt_scalef32_pk_fp8_f32 v39, v146, v147, s48
	v_cvt_scalef32_pk_fp8_f32 v36, v58, v59, s48
	v_cvt_scalef32_pk_fp8_f32 v40, v42, v43, s48
	v_cvt_scalef32_pk_fp8_f32 v37, v62, v63, s48
	v_cvt_scalef32_pk_fp8_f32 v41, v46, v47, s48
	v_cvt_scalef32_pk_fp8_f32 v34, v52, v53, s48 op_sel:[0,0,0,1]
	v_cvt_scalef32_pk_fp8_f32 v38, v126, v127, s48 op_sel:[0,0,0,1]
	v_cvt_scalef32_pk_fp8_f32 v35, v56, v57, s48 op_sel:[0,0,0,1]
	v_cvt_scalef32_pk_fp8_f32 v39, v148, v149, s48 op_sel:[0,0,0,1]
	v_cvt_scalef32_pk_fp8_f32 v36, v60, v61, s48 op_sel:[0,0,0,1]
	v_cvt_scalef32_pk_fp8_f32 v40, v44, v45, s48 op_sel:[0,0,0,1]
	v_cvt_scalef32_pk_fp8_f32 v37, v64, v65, s48 op_sel:[0,0,0,1]
	s_waitcnt lgkmcnt(4)
	v_mfma_f32_32x32x64_f8f6f4 v[82:97], v[82:89], v[98:105], 0
	v_cvt_scalef32_pk_fp8_f32 v41, v48, v49, s48 op_sel:[0,0,0,1]
	v_add_f32_e64 v110, v110, v52
	v_add_f32_e64 v111, v111, v53
	v_add_f32_e64 v50, v108, v50
	v_add_f32_e64 v51, v109, v51
	s_addk_i32 s6, 0x4680
	v_add_f32_e64 v52, v56, v110
	v_add_f32_e64 v53, v57, v111
	v_add_f32_e64 v50, v54, v50
	v_add_f32_e64 v51, v55, v51
	s_cmp_lg_u32 s8, 2
	v_add_f32_e64 v50, v58, v50
	v_add_f32_e64 v51, v59, v51
	v_pk_add_f32 v[52:53], v[60:61], v[52:53]
	s_cselect_b32 s4, s6, 0
	v_pk_add_f32 v[52:53], v[64:65], v[52:53]
	v_pk_add_f32 v[50:51], v[62:63], v[50:51]
	s_add_i32 s4, s4, 0
	v_pk_add_f32 v[50:51], v[124:125], v[50:51]
	v_pk_add_f32 v[52:53], v[126:127], v[52:53]
	s_waitcnt lgkmcnt(2)
	v_mfma_f32_32x32x64_f8f6f4 v[18:33], v[116:123], v[34:41], v[18:33]
	v_add_f32_e64 v52, v148, v52
	v_add_f32_e64 v53, v149, v53
	v_add_f32_e64 v50, v146, v50
	v_add_f32_e64 v51, v147, v51
	v_add_f32_e64 v44, v44, v52
	v_add_f32_e64 v45, v45, v53
	v_add_f32_e64 v42, v42, v50
	v_add_f32_e64 v43, v43, v51
	v_add_f32_e64 v110, v48, v44
	v_add_f32_e64 v111, v49, v45
	v_add_f32_e64 v108, v46, v42
	v_add_f32_e64 v109, v47, v43
	s_waitcnt lgkmcnt(0)
	v_mfma_f32_32x32x64_f8f6f4 v[2:17], v[138:145], v[34:41], v[2:17]
	v_add_u32_e32 v34, s4, v155
	s_waitcnt vmcnt(3)
	ds_write_b64 v34, v[112:113]
	v_add_u32_e32 v34, s4, v238
	s_waitcnt vmcnt(2)
	ds_write2_b32 v34, v114, v115 offset1:8
	s_waitcnt lgkmcnt(0)
	s_barrier

; DI f32x16 mfma8(v8i a, v8i b, f32x16 c) { return __builtin_amdgcn_mfma_scale_f32_32x32x64_f8f6f4(a, b, c, 0, 0, 0, 0, 0, 0); }
; DI void attn_unit_a8(unsigned char* lds, const AttnArgs& a) {
;     ...
;     auto gload = [&](int t, u32x2& kreg, u32x2& vreg) __attribute__((always_inline)) {
;         const unsigned char* kp = (t < 64) ? a.klat8 + (size_t)(t * 64 + lrow) * 128 : a.kctx8 + (size_t)((t - 64) * 64 + lrow) * 128;
;         kreg = *(const u32x2*)(kp + 8 * lch);
;         vreg = *(const u32x2*)(vsrc + (size_t)t * 64);
;     };
;     auto lstore = [&](int slot, const u32x2& kreg, const u32x2& vreg) __attribute__((always_inline)) { unsigned char* b = lds + slot * AT_BUFB;
;         *(u32x2*)(b + ldk) = kreg; *(unsigned*)(b + ldv) = vreg.x; *(unsigned*)(b + ldv + 32) = vreg.y; };
;     ...
;     auto step = [&](int t, u32x2& kl, u32x2& vl, const u32x2& ks, const u32x2& vs, f32x16& c0, f32x16& c1, f32x16& n0, f32x16& n1, const int hk, const int wj) __attribute__((always_inline)) {
;         const int slot1 = slot == 2 ? 0 : slot + 1, slot2 = slot1 == 2 ? 0 : slot1 + 1;
;         if (hk == 1) { w_cvt(); w_issue(wj + 1 < AT_NWT ? wj + 1 : AT_NWT - 1); }
;         if (hk == 2) w_store(wj);
;         { const int tn = t + 3; gload(tn < a.t1 ? tn : a.t1 - 1, kl, vl); }
;         const unsigned char* Kb = lds + slot * AT_BUFB; const unsigned char* Kn = lds + slot1 * AT_BUFB;
;         const v8i k0 = kread(Kn, 0), k1 = kread(Kn, 1), v0 = vread(Kb, 0), v1 = vread(Kb, 1);
;         n0 = mfma8(k0, qf8, cinit); n1 = mfma8(k1, qf8, cinit);
;         expsum(c0); expsum(c1);
;         const v8i P = pack8(c0, c1);
;         o0[0] = mfma8(v0, P, o0[0]); o0[1] = mfma8(v1, P, o0[1]);
;         lstore(slot2, ks, vs);
;         __syncthreads();
;         slot = slot1;
;     };
.LBB0_1933:
	s_lshl_b32 s10, s75, 8
	s_ashr_i32 s11, s10, 31
	s_lshl_b64 s[10:11], s[10:11], 7
	s_add_u32 s8, s54, s10
	s_addc_u32 s10, s55, s11
	s_add_u32 s8, s8, s77
	s_addc_u32 s10, s10, 0
	s_add_u32 s12, s8, 0x400000
	s_addc_u32 s13, s10, 0
	s_mov_b32 s14, 0
	v_mov_b64_e32 v[80:81], v[64:65]
	v_mov_b64_e32 v[78:79], v[62:63]
	v_mov_b64_e32 v[76:77], v[60:61]
	v_mov_b64_e32 v[74:75], v[58:59]
	v_mov_b64_e32 v[72:73], v[56:57]
	v_mov_b64_e32 v[70:71], v[54:55]
	v_mov_b64_e32 v[68:69], v[52:53]
	v_mov_b64_e32 v[66:67], v[50:51]
	v_mov_b64_e32 v[96:97], v[48:49]
	v_mov_b64_e32 v[94:95], v[46:47]
	v_mov_b64_e32 v[92:93], v[44:45]
	v_mov_b64_e32 v[90:91], v[42:43]
	v_mov_b64_e32 v[88:89], v[40:41]
	v_mov_b64_e32 v[86:87], v[38:39]
	v_mov_b64_e32 v[84:85], v[36:37]
	v_mov_b64_e32 v[82:83], v[34:35]
	v_mov_b32_e32 v236, v130
	v_ashrrev_i32_e32 v237, 31, v130
	v_lshlrev_b64 v[236:237], 7, v[236:237]
	v_lshl_add_u64 v[236:237], v[236:237], 0, v[132:133]
	v_add_u32_e32 v238, 0x1400, v168
.LBB0_1934:
	s_min_u32 s8, s50, 64
	s_cmp_lt_u32 s50, 61
	s_cselect_b64 s[10:11], -1, 0
	s_lshl_b32 s8, s8, 6
	s_add_i32 s15, s8, 0xc0
	s_add_i32 s18, s8, 0xfffff0c0
	s_and_b64 s[16:17], s[10:11], exec
	s_cselect_b32 s15, s15, s18
	s_lshl_b32 s82, s15, 7
	s_mov_b32 s18, s14
	s_add_i32 s14, s14, 1
	s_cmp_lg_u32 s18, 2
	s_cselect_b32 s14, s14, 0
	s_mul_i32 s19, s14, 0x4680
	v_add_u32_e32 v106, s19, v169
	ds_read_b128 v[50:53], v106
	ds_read_b128 v[54:57], v106 offset:16
	s_and_b64 s[10:11], s[10:11], exec
	s_cselect_b32 s16, s42, s12
	s_cselect_b32 s17, s43, s13
	s_waitcnt lgkmcnt(0)
	v_mfma_f32_32x32x64_f8f6f4 v[34:49], v[50:57], v[98:105], 0
	s_add_u32 s82, s16, s82
	s_addc_u32 s83, s17, 0
	v_lshl_add_u64 v[50:51], v[236:237], 0, s[82:83]
	v_lshl_add_u64 v[58:59], v[134:135], 0, s[8:9]
	global_load_dwordx2 v[112:113], v[50:51], off
	ds_read_b128 v[50:53], v106 offset:2560
	ds_read_b128 v[54:57], v106 offset:2576
	global_load_dwordx2 v[114:115], v[58:59], off offset:192
	s_mulk_i32 s18, 0x4680
	v_add_u32_e32 v58, s18, v169
	v_exp_f32_e32 v82, v82
	v_exp_f32_e32 v83, v83
	v_exp_f32_e32 v86, v86
	v_exp_f32_e32 v87, v87
	v_exp_f32_e32 v90, v90
	v_exp_f32_e32 v91, v91
	v_exp_f32_e32 v94, v94
	v_exp_f32_e32 v95, v95
	v_exp_f32_e32 v124, v66
	v_exp_f32_e32 v125, v67
	v_exp_f32_e32 v148, v70
	v_exp_f32_e32 v149, v71
	v_exp_f32_e32 v74, v74
	v_exp_f32_e32 v75, v75
	v_exp_f32_e32 v78, v78
	v_exp_f32_e32 v79, v79
	ds_read_b128 v[116:119], v58 offset:5120
	ds_read_b128 v[120:123], v58 offset:5136
	ds_read_b128 v[140:143], v58 offset:7680
	ds_read_b128 v[144:147], v58 offset:7696
	v_exp_f32_e32 v84, v84
	v_exp_f32_e32 v85, v85
	v_exp_f32_e32 v88, v88
	v_exp_f32_e32 v89, v89
	v_exp_f32_e32 v92, v92
	v_exp_f32_e32 v93, v93
	v_exp_f32_e32 v96, v96
	v_exp_f32_e32 v97, v97
	v_exp_f32_e32 v126, v68
	v_exp_f32_e32 v127, v69
	v_exp_f32_e32 v150, v72
	v_exp_f32_e32 v151, v73
	v_exp_f32_e32 v76, v76
	v_exp_f32_e32 v77, v77
	v_exp_f32_e32 v80, v80
	v_exp_f32_e32 v81, v81
	v_cvt_scalef32_pk_fp8_f32 v66, v82, v83, s69
	v_cvt_scalef32_pk_fp8_f32 v70, v124, v125, s69
	v_cvt_scalef32_pk_fp8_f32 v67, v86, v87, s69
	v_cvt_scalef32_pk_fp8_f32 v71, v148, v149, s69
	v_cvt_scalef32_pk_fp8_f32 v68, v90, v91, s69
	v_cvt_scalef32_pk_fp8_f32 v72, v74, v75, s69
	v_cvt_scalef32_pk_fp8_f32 v69, v94, v95, s69
	v_cvt_scalef32_pk_fp8_f32 v73, v78, v79, s69
	v_cvt_scalef32_pk_fp8_f32 v66, v84, v85, s69 op_sel:[0,0,0,1]
	v_cvt_scalef32_pk_fp8_f32 v70, v126, v127, s69 op_sel:[0,0,0,1]
	v_cvt_scalef32_pk_fp8_f32 v67, v88, v89, s69 op_sel:[0,0,0,1]
	v_cvt_scalef32_pk_fp8_f32 v71, v150, v151, s69 op_sel:[0,0,0,1]
	v_cvt_scalef32_pk_fp8_f32 v68, v92, v93, s69 op_sel:[0,0,0,1]
	v_cvt_scalef32_pk_fp8_f32 v72, v76, v77, s69 op_sel:[0,0,0,1]
	v_cvt_scalef32_pk_fp8_f32 v69, v96, v97, s69 op_sel:[0,0,0,1]
	v_cvt_scalef32_pk_fp8_f32 v73, v80, v81, s69 op_sel:[0,0,0,1]
	s_waitcnt lgkmcnt(4)
	v_mfma_f32_32x32x64_f8f6f4 v[50:65], v[50:57], v[98:105], 0
	s_add_i32 s15, s19, 0x4680
	s_cmp_eq_u32 s14, 2
	v_add_f32_e64 v110, v110, v84
	v_add_f32_e64 v111, v111, v85
	v_add_f32_e64 v82, v108, v82
	v_add_f32_e64 v83, v109, v83
	s_cselect_b64 s[10:11], -1, 0
	v_add_f32_e64 v84, v88, v110
	v_add_f32_e64 v85, v89, v111
	v_add_f32_e64 v82, v86, v82
	v_add_f32_e64 v83, v87, v83
	v_add_f32_e64 v84, v92, v84
	v_add_f32_e64 v85, v93, v85
	v_pk_add_f32 v[82:83], v[90:91], v[82:83]
	s_and_b64 s[16:17], s[10:11], exec
	v_pk_add_f32 v[84:85], v[96:97], v[84:85]
	v_pk_add_f32 v[82:83], v[94:95], v[82:83]
	s_cselect_b32 s8, 0, s15
	v_pk_add_f32 v[82:83], v[124:125], v[82:83]
	v_pk_add_f32 v[84:85], v[126:127], v[84:85]
	s_waitcnt lgkmcnt(2)
	v_mfma_f32_32x32x64_f8f6f4 v[18:33], v[116:123], v[66:73], v[18:33]
	s_add_i32 s8, s8, 0
	v_add_f32_e64 v84, v150, v84
	v_add_f32_e64 v85, v151, v85
	v_add_f32_e64 v82, v148, v82
	v_add_f32_e64 v83, v149, v83
	v_add_f32_e64 v76, v76, v84
	v_add_f32_e64 v77, v77, v85
	v_add_f32_e64 v74, v74, v82
	v_add_f32_e64 v75, v75, v83
	v_add_f32_e64 v110, v80, v76
	v_add_f32_e64 v111, v81, v77
	v_add_f32_e64 v108, v78, v74
	v_add_f32_e64 v109, v79, v75
	s_cmpk_gt_u32 s50, 0x42
	s_waitcnt lgkmcnt(0)
	v_mfma_f32_32x32x64_f8f6f4 v[2:17], v[140:147], v[66:73], v[2:17]
	v_add_u32_e32 v66, s8, v131
	s_waitcnt vmcnt(3)
	ds_write_b64 v66, v[136:137]
	v_add_u32_e32 v66, s8, v238
	s_waitcnt vmcnt(2)
	ds_write2_b32 v66, v138, v139 offset1:8
	s_waitcnt lgkmcnt(0)
	s_barrier
; DI f32x16 mfma8(v8i a, v8i b, f32x16 c) { return __builtin_amdgcn_mfma_scale_f32_32x32x64_f8f6f4(a, b, c, 0, 0, 0, 0, 0, 0); }
; DI void attn_unit_a8(unsigned char* lds, const AttnArgs& a) {
;     ...
;     auto gload = [&](int t, u32x2& kreg, u32x2& vreg) __attribute__((always_inline)) {
;         const unsigned char* kp = (t < 64) ? a.klat8 + (size_t)(t * 64 + lrow) * 128 : a.kctx8 + (size_t)((t - 64) * 64 + lrow) * 128;
;         kreg = *(const u32x2*)(kp + 8 * lch);
;         vreg = *(const u32x2*)(vsrc + (size_t)t * 64);
;     };
;     auto lstore = [&](int slot, const u32x2& kreg, const u32x2& vreg) __attribute__((always_inline)) { unsigned char* b = lds + slot * AT_BUFB;
;         *(u32x2*)(b + ldk) = kreg; *(unsigned*)(b + ldv) = vreg.x; *(unsigned*)(b + ldv + 32) = vreg.y; };
;     ...
;     auto step = [&](int t, u32x2& kl, u32x2& vl, const u32x2& ks, const u32x2& vs, f32x16& c0, f32x16& c1, f32x16& n0, f32x16& n1, const int hk, const int wj) __attribute__((always_inline)) {
;         const int slot1 = slot == 2 ? 0 : slot + 1, slot2 = slot1 == 2 ? 0 : slot1 + 1;
;         if (hk == 1) { w_cvt(); w_issue(wj + 1 < AT_NWT ? wj + 1 : AT_NWT - 1); }
;         if (hk == 2) w_store(wj);
;         { const int tn = t + 3; gload(tn < a.t1 ? tn : a.t1 - 1, kl, vl); }
;         const unsigned char* Kb = lds + slot * AT_BUFB; const unsigned char* Kn = lds + slot1 * AT_BUFB;
;         const v8i k0 = kread(Kn, 0), k1 = kread(Kn, 1), v0 = vread(Kb, 0), v1 = vread(Kb, 1);
;         n0 = mfma8(k0, qf8, cinit); n1 = mfma8(k1, qf8, cinit);
;         expsum(c0); expsum(c1);
;         const v8i P = pack8(c0, c1);
;         o0[0] = mfma8(v0, P, o0[0]); o0[1] = mfma8(v1, P, o0[1]);
;         lstore(slot2, ks, vs);
;         __syncthreads();
;         slot = slot1;
;     };
	s_cbranch_scc1 .LBB0_1936
	s_min_u32 s8, s50, 63
	s_cmp_lt_u32 s50, 60
	s_cselect_b64 s[16:17], -1, 0
	s_lshl_b32 s8, s8, 6
	s_add_i32 s15, s8, 0x100
	s_add_i32 s20, s8, 0xfffff100
	s_and_b64 s[18:19], s[16:17], exec
	s_cselect_b32 s15, s15, s20
	s_lshl_b32 s84, s15, 7
	s_add_i32 s14, s14, 1
	s_and_b64 s[10:11], s[10:11], exec
	s_cselect_b32 s14, 0, s14
	s_and_b64 s[16:17], s[16:17], exec
	s_cselect_b32 s17, s43, s13
	s_cselect_b32 s16, s42, s12
	s_mul_i32 s10, s14, 0x4680
	s_add_u32 s84, s16, s84
	s_addc_u32 s85, s17, 0
	v_add_u32_e32 v86, s10, v169
	v_lshl_add_u64 v[90:91], v[236:237], 0, s[84:85]
	ds_read_b128 v[66:69], v86 offset:2560
	ds_read_b128 v[70:73], v86 offset:2576
	ds_read_b128 v[82:85], v86
	ds_read_b128 v[86:89], v86 offset:16
	global_load_dwordx2 v[136:137], v[90:91], off
	v_lshl_add_u64 v[90:91], v[134:135], 0, s[8:9]
	global_load_dwordx2 v[138:139], v[90:91], off offset:256
	v_exp_f32_e32 v124, v34
	v_exp_f32_e32 v125, v35
	v_exp_f32_e32 v36, v36
	v_exp_f32_e32 v37, v37
	v_exp_f32_e32 v126, v38
	v_exp_f32_e32 v127, v39
	v_exp_f32_e32 v42, v42
	v_exp_f32_e32 v43, v43
	v_exp_f32_e32 v46, v46
	v_exp_f32_e32 v47, v47
	v_exp_f32_e32 v50, v50
	v_exp_f32_e32 v51, v51
	v_exp_f32_e32 v54, v54
	v_exp_f32_e32 v55, v55
	v_exp_f32_e32 v58, v58
	v_exp_f32_e32 v59, v59
	v_exp_f32_e32 v62, v62
	v_exp_f32_e32 v63, v63
	ds_read_b128 v[116:119], v106 offset:5120
	ds_read_b128 v[120:123], v106 offset:5136
	ds_read_b128 v[140:143], v106 offset:7680
	ds_read_b128 v[144:147], v106 offset:7696
	v_exp_f32_e32 v148, v40
	v_exp_f32_e32 v149, v41
	v_exp_f32_e32 v44, v44
	v_exp_f32_e32 v45, v45
	v_exp_f32_e32 v48, v48
	v_exp_f32_e32 v49, v49
	v_exp_f32_e32 v52, v52
	v_exp_f32_e32 v53, v53
	v_exp_f32_e32 v56, v56
	v_exp_f32_e32 v57, v57
	v_exp_f32_e32 v60, v60
	v_exp_f32_e32 v61, v61
	v_exp_f32_e32 v64, v64
	v_exp_f32_e32 v65, v65
	v_cvt_scalef32_pk_fp8_f32 v34, v124, v125, s69
	v_pk_add_f32 v[110:111], v[110:111], v[36:37]
	v_cvt_scalef32_pk_fp8_f32 v34, v36, v37, s69 op_sel:[0,0,0,1]
	s_waitcnt lgkmcnt(6)
	v_mfma_f32_32x32x64_f8f6f4 v[66:81], v[66:73], v[98:105], 0
	v_cvt_scalef32_pk_fp8_f32 v38, v50, v51, s69
	v_cvt_scalef32_pk_fp8_f32 v35, v126, v127, s69
	v_cvt_scalef32_pk_fp8_f32 v39, v54, v55, s69
	v_cvt_scalef32_pk_fp8_f32 v36, v42, v43, s69
	v_cvt_scalef32_pk_fp8_f32 v40, v58, v59, s69
	v_cvt_scalef32_pk_fp8_f32 v37, v46, v47, s69
	v_cvt_scalef32_pk_fp8_f32 v41, v62, v63, s69
	v_cvt_scalef32_pk_fp8_f32 v38, v52, v53, s69 op_sel:[0,0,0,1]
	v_cvt_scalef32_pk_fp8_f32 v35, v148, v149, s69 op_sel:[0,0,0,1]
	v_cvt_scalef32_pk_fp8_f32 v39, v56, v57, s69 op_sel:[0,0,0,1]
	v_cvt_scalef32_pk_fp8_f32 v36, v44, v45, s69 op_sel:[0,0,0,1]
	v_cvt_scalef32_pk_fp8_f32 v40, v60, v61, s69 op_sel:[0,0,0,1]
	v_cvt_scalef32_pk_fp8_f32 v37, v48, v49, s69 op_sel:[0,0,0,1]
	v_cvt_scalef32_pk_fp8_f32 v41, v64, v65, s69 op_sel:[0,0,0,1]
	v_pk_add_f32 v[108:109], v[108:109], v[124:125]
	s_waitcnt lgkmcnt(4)
	v_mfma_f32_32x32x64_f8f6f4 v[82:97], v[82:89], v[98:105], 0
	s_addk_i32 s10, 0x4680
	v_add_f32_e64 v110, v148, v110
	v_add_f32_e64 v111, v149, v111
	v_add_f32_e64 v108, v126, v108
	v_add_f32_e64 v109, v127, v109
	s_cmp_lg_u32 s14, 2
	v_add_f32_e64 v42, v42, v108
	v_add_f32_e64 v43, v43, v109
	v_add_f32_e64 v44, v44, v110
	v_add_f32_e64 v45, v45, v111
	s_cselect_b32 s8, s10, 0
	v_add_f32_e64 v44, v48, v44
	v_add_f32_e64 v45, v49, v45
	v_pk_add_f32 v[42:43], v[46:47], v[42:43]
	s_add_i32 s8, s8, 0
	v_pk_add_f32 v[42:43], v[50:51], v[42:43]
	v_pk_add_f32 v[44:45], v[52:53], v[44:45]
	v_pk_add_f32 v[42:43], v[54:55], v[42:43]
	v_pk_add_f32 v[44:45], v[56:57], v[44:45]
	v_pk_add_f32 v[42:43], v[58:59], v[42:43]
	s_waitcnt lgkmcnt(2)
	v_mfma_f32_32x32x64_f8f6f4 v[18:33], v[116:123], v[34:41], v[18:33]
	v_add_f32_e64 v44, v60, v44
	v_add_f32_e64 v45, v61, v45
	v_add_f32_e64 v108, v62, v42
	v_add_f32_e64 v109, v63, v43
	v_add_f32_e64 v110, v64, v44
	v_add_f32_e64 v111, v65, v45
	s_waitcnt lgkmcnt(0)
	v_mfma_f32_32x32x64_f8f6f4 v[2:17], v[140:147], v[34:41], v[2:17]
	v_add_u32_e32 v34, s8, v131
	s_waitcnt vmcnt(3)
	ds_write_b64 v34, v[112:113]
	v_add_u32_e32 v34, s8, v238
	s_waitcnt vmcnt(2)
	ds_write2_b32 v34, v114, v115 offset1:8
	s_waitcnt lgkmcnt(0)
	s_barrier
